# STEP range checks read p.lo/p.hi from SGPRs s100/s101 (cached once at kernel start) instead of two serial LDS reads per STEP (on top of v48)
# speedup vs baseline: 1.0167x; 1.0031x over previous
.LBB0_5:
	s_or_b64 exec, exec, s[0:1]
	s_add_i32 s0, 0, 0x25ff0
	v_mov_b32 v0, s0
	ds_read_b32 v0, v0 offset:8
	v_mov_b32 v1, s0
	ds_read_b32 v1, v1 offset:12
	v_writelane_b32 v250, s0, 4
	s_lshr_b32 s43, s28, 6
	s_waitcnt lgkmcnt(1)
	v_readfirstlane_b32 s0, v0
	s_mov_b32 s100, s0
	s_cmp_lt_i32 s0, 1
	s_waitcnt lgkmcnt(0)
	v_readfirstlane_b32 s26, v1
	s_mov_b32 s101, s26
	s_cselect_b64 s[0:1], -1, 0
	s_cmp_gt_i32 s26, 0
	s_cselect_b64 s[2:3], -1, 0
	s_and_b64 s[0:1], s[0:1], s[2:3]
	s_andn2_b64 vcc, exec, s[0:1]
	s_cbranch_vccnz .LBB0_136
	s_cmpk_gt_i32 s94, 0x18df
	v_mbcnt_lo_u32_b32 v74, -1, 0
	v_mbcnt_hi_u32_b32 v74, -1, v74
	v_lshl_add_u32 v64, s43, 6, v74
	s_cbranch_scc1 .LBB0_32
	v_lshlrev_b32_e32 v0, 2, v64
	v_and_b32_e32 v65, 0xfc, v0
	v_ashrrev_i32_e32 v0, 3, v64
	s_movk_i32 s2, 0x110
	v_ashrrev_i32_e32 v76, 4, v64
	v_and_b32_e32 v75, -8, v0
	v_mul_lo_u32 v0, v76, s2
	v_add_u32_e32 v2, 0x200, v64
	v_add_u32_e32 v77, 0, v0
	v_lshlrev_b32_e32 v0, 4, v64
	v_ashrrev_i32_e32 v78, 4, v2
	v_add_u32_e32 v3, 0x400, v64
	v_and_b32_e32 v66, 0xf0, v0
	v_mul_lo_u32 v0, v78, s2
	v_ashrrev_i32_e32 v80, 4, v3
	v_add_u32_e32 v4, 0x600, v64
	v_add_u32_e32 v79, 0, v0
	v_mul_lo_u32 v0, v80, s2
	v_ashrrev_i32_e32 v82, 4, v4
	v_add_u32_e32 v5, 0x800, v64
	v_add_u32_e32 v81, 0, v0
	v_mul_lo_u32 v0, v82, s2
	v_ashrrev_i32_e32 v84, 4, v5
	v_add_u32_e32 v6, 0xa00, v64
	v_add_u32_e32 v83, 0, v0
	v_mul_lo_u32 v0, v84, s2
	v_ashrrev_i32_e32 v86, 4, v6
	v_add_u32_e32 v7, 0xc00, v64
	v_add_u32_e32 v85, 0, v0
	v_mul_lo_u32 v0, v86, s2
	v_ashrrev_i32_e32 v88, 4, v7
	v_add_u32_e32 v87, 0, v0
	v_mul_lo_u32 v0, v88, s2
	v_add_u32_e32 v89, 0, v0
	v_lshlrev_b32_e32 v0, 3, v64
	s_movk_i32 s4, 0x210
	v_and_b32_e32 v0, 0xf8, v0
	v_ashrrev_i32_e32 v93, 5, v2
	v_lshlrev_b32_e32 v11, 1, v0
	v_mul_lo_u32 v2, v93, s4
	v_ashrrev_i32_e32 v95, 5, v3
	v_add3_u32 v94, 0, v2, v11
	v_mul_lo_u32 v2, v95, s4
	v_ashrrev_i32_e32 v97, 5, v4
	v_add3_u32 v96, 0, v2, v11
	v_mul_lo_u32 v2, v97, s4
	v_ashrrev_i32_e32 v99, 5, v5
	v_add3_u32 v98, 0, v2, v11
	v_mul_lo_u32 v2, v99, s4
	v_ashrrev_i32_e32 v101, 5, v6
	v_add_u32_e32 v8, 0xe00, v64
	v_add3_u32 v100, 0, v2, v11
	v_mul_lo_u32 v2, v101, s4
	v_ashrrev_i32_e32 v103, 5, v7
	v_add3_u32 v102, 0, v2, v11
	v_mul_lo_u32 v2, v103, s4
	v_ashrrev_i32_e32 v105, 5, v8
	v_add3_u32 v104, 0, v2, v11
	v_mul_lo_u32 v2, v105, s4
	v_add3_u32 v106, 0, v2, v11
	v_add_u32_e32 v2, 0x1000, v64
	v_ashrrev_i32_e32 v107, 5, v2
	v_mul_lo_u32 v2, v107, s4
	v_add3_u32 v108, 0, v2, v11
	v_add_u32_e32 v2, 0x1200, v64
	v_ashrrev_i32_e32 v109, 5, v2
	v_mul_lo_u32 v2, v109, s4
	v_add3_u32 v110, 0, v2, v11
	v_add_u32_e32 v2, 0x1400, v64
	v_ashrrev_i32_e32 v111, 5, v2
	v_mul_lo_u32 v2, v111, s4
	v_add3_u32 v112, 0, v2, v11
	v_add_u32_e32 v2, 0x1600, v64
	v_ashrrev_i32_e32 v113, 5, v2
	v_mul_lo_u32 v2, v113, s4
	v_add3_u32 v114, 0, v2, v11
	v_add_u32_e32 v2, 0x1800, v64
	v_ashrrev_i32_e32 v115, 5, v2
	v_mul_lo_u32 v2, v115, s4
	v_add3_u32 v116, 0, v2, v11
	v_add_u32_e32 v2, 0x1a00, v64
	v_ashrrev_i32_e32 v117, 5, v2
	v_mul_lo_u32 v2, v117, s4
	s_cmpk_eq_i32 s37, 0x100
	v_add3_u32 v118, 0, v2, v11
	v_add_u32_e32 v2, 0x1c00, v64
	s_cselect_b64 s[0:1], -1, 0
	s_add_u32 s18, s60, 0x21c10000
	v_ashrrev_i32_e32 v119, 5, v2
	s_addc_u32 s19, s61, 0
	v_mul_lo_u32 v2, v119, s4
	s_load_dwordx2 s[6:7], s[70:71], 0x108
	s_load_dwordx2 s[8:9], s[70:71], 0xf8
	s_load_dwordx2 s[10:11], s[70:71], 0xd8
	s_load_dwordx2 s[12:13], s[70:71], 0x38
	v_add3_u32 v120, 0, v2, v11
	v_add_u32_e32 v2, 0x1e00, v64
	s_add_u32 s21, s60, 0x1c10000
	v_ashrrev_i32_e32 v121, 5, v2
	s_addc_u32 s22, s61, 0
	v_mul_lo_u32 v2, v121, s4
	s_add_u32 s23, s60, 0x1410000
	v_ashrrev_i32_e32 v90, 4, v8
	v_lshlrev_b32_e32 v9, 1, v75
	v_ashrrev_i32_e32 v91, 5, v64
	v_add3_u32 v122, 0, v2, v11
	v_mul_u32_u24_e32 v2, 0x210, v65
	s_addc_u32 s24, s61, 0
	v_mul_u32_u24_e32 v1, 0x110, v65
	v_mov_b32_e32 v69, 0
	v_mul_lo_u32 v10, v91, s4
	v_add3_u32 v123, 0, v9, v2
	v_mul_lo_u32 v2, v90, s2
	s_movk_i32 s2, 0x80
	s_add_u32 s25, s60, 0x10000
	s_mov_b32 s3, 0
	v_mov_b32_e32 v67, v69
	s_movk_i32 s20, 0x600
	v_add3_u32 v92, 0, v10, v11
	v_add_u32_e32 v124, 0, v2
	v_cmp_gt_u32_e64 s[4:5], s2, v65
	s_addc_u32 s27, s61, 0
	v_add3_u32 v125, 0, v75, v1
	v_lshlrev_b32_e32 v70, 1, v0
	s_movk_i32 s29, 0x2840
	s_mov_b32 s30, s94
	v_add_u32_e32 v126, 0x380, v65
	s_branch .LBB0_9

.LBB0_136:
	v_readlane_b32 s0, v250, 4
	s_waitcnt lgkmcnt(0)
	s_mov_b32 s0, s100
	s_cmp_lt_i32 s0, 2
	s_mov_b32 s26, s101
	s_cselect_b64 s[0:1], -1, 0
	s_cmp_gt_i32 s26, 1
	s_cselect_b64 s[2:3], -1, 0
	s_and_b64 s[0:1], s[0:1], s[2:3]
	s_andn2_b64 vcc, exec, s[0:1]
	s_cbranch_vccnz .LBB0_217
	s_cmpk_gt_i32 s94, 0xff
	v_mbcnt_lo_u32_b32 v0, -1, 0
	v_mbcnt_hi_u32_b32 v0, -1, v0
	v_lshl_add_u32 v12, s43, 6, v0
	s_cbranch_scc1 .LBB0_163
	s_movk_i32 s0, 0x420
	v_bfe_u32 v4, v12, 4, 4
	v_cmp_gt_i32_e32 vcc, s0, v12
	s_movk_i32 s0, 0x200
	v_and_b32_e32 v5, 15, v12
	v_lshlrev_b32_e32 v0, 6, v4
	v_mov_b32_e32 v1, 0
	v_cmp_gt_i32_e64 s[4:5], s0, v12
	s_movk_i32 s0, 0x400
	v_lshl_add_u64 v[2:3], s[60:61], 0, v[0:1]
	v_lshlrev_b32_e32 v0, 2, v5
	s_load_dwordx4 s[8:11], s[70:71], 0xa8
	s_add_u32 s27, s60, 0x31ce8000
	v_cmp_gt_i32_e64 s[6:7], s0, v12
	v_lshl_add_u64 v[0:1], v[2:3], 0, v[0:1]
	s_mov_b64 s[0:1], 0x31ff8000
	v_ashrrev_i32_e32 v13, 31, v12
	s_mov_b64 s[2:3], 0x31ce8000
	s_addc_u32 s29, s61, 0
	s_mov_b64 s[12:13], 0x31ef8000
	v_lshl_add_u64 v[16:17], v[0:1], 0, s[0:1]
	v_lshl_add_u64 v[0:1], v[12:13], 4, s[60:61]
	s_add_u32 s30, s60, 0x31ef8000
	v_lshl_add_u64 v[18:19], v[0:1], 0, s[2:3]
	v_lshl_add_u64 v[20:21], v[0:1], 0, s[12:13]
	v_lshl_add_u32 v0, v12, 3, 0
	s_addc_u32 s31, s61, 0
	v_add_u32_e32 v30, 0x6200, v0
	v_lshlrev_b64 v[0:1], 2, v[12:13]
	s_waitcnt lgkmcnt(0)
	v_lshl_add_u64 v[22:23], s[8:9], 0, v[0:1]
	v_lshl_add_u64 v[24:25], s[10:11], 0, v[0:1]
	v_lshl_add_u32 v0, v4, 9, 0
	s_bitcmp1_b32 s94, 0
	v_ashrrev_i32_e32 v14, 8, v12
	v_lshl_add_u32 v28, v12, 4, 0
	v_add_u32_e32 v13, 0x6200, v0
	v_lshl_add_u32 v0, v5, 3, 0
	s_cselect_b64 s[2:3], -1, 0
	s_bitcmp1_b32 s37, 0
	v_ashrrev_i32_e32 v15, 31, v14
	s_mov_b32 s1, 0
	v_add_u32_e32 v29, 0x4200, v28
	s_movk_i32 s33, 0xfe00
	v_add_u32_e32 v31, 0xfffffe00, v12
	v_add_u32_e32 v32, 0x4200, v0
	v_lshl_add_u32 v33, v14, 3, 0
	s_cselect_b64 s[10:11], -1, 0
	s_movk_i32 s34, 0x220
	s_movk_i32 s35, 0xfe20
	s_mov_b64 s[12:13], 0x8000
	s_movk_i32 s36, 0xfc1f
	s_movk_i32 s38, 0x1ff
	s_movk_i32 s39, 0xfc00
	s_movk_i32 s40, 0xf9ff
	s_mov_b64 s[14:15], 0x800
	v_mov_b32_e32 v34, 0x4200
	s_mov_b32 s41, s94

.LBB0_217:
	v_readlane_b32 s0, v250, 4
	s_mov_b32 s45, 0
	s_waitcnt lgkmcnt(1)
	s_mov_b32 s0, s100
	s_cmp_lt_i32 s0, 3
	s_waitcnt lgkmcnt(0)
	s_mov_b32 s29, s101
	s_cselect_b64 s[0:1], -1, 0
	s_cmp_gt_i32 s29, 2
	s_cselect_b64 s[2:3], -1, 0
	s_and_b64 s[0:1], s[0:1], s[2:3]
	s_andn2_b64 vcc, exec, s[0:1]
	s_cbranch_vccnz .LBB0_336
	s_cmpk_gt_i32 s94, 0xff
	v_mbcnt_lo_u32_b32 v0, -1, 0
	v_mbcnt_hi_u32_b32 v0, -1, v0
	v_lshl_add_u32 v14, s43, 6, v0
	s_cbranch_scc1 .LBB0_282
	s_movk_i32 s0, 0x1000
	s_add_u32 s30, s60, 0x31ff8000
	v_cmp_gt_i32_e32 vcc, s0, v14
	s_movk_i32 s0, 0x840
	s_addc_u32 s31, s61, 0
	v_cmp_gt_i32_e64 s[4:5], s0, v14
	s_movk_i32 s0, 0x400
	s_add_u32 s33, s60, 0x31ce8000
	v_cmp_gt_i32_e64 s[6:7], s0, v14
	s_movk_i32 s0, 0x3000
	s_addc_u32 s34, s61, 0
	v_cmp_gt_i32_e64 s[10:11], s0, v14
	s_load_dwordx4 s[12:15], s[70:71], 0xa8
	s_load_dwordx2 s[0:1], s[70:71], 0xb8
	s_add_u32 s35, s60, 0x31ef8000
	v_ashrrev_i32_e32 v15, 31, v14
	s_mov_b64 s[2:3], 0x31ff8000
	s_addc_u32 s36, s61, 0
	s_add_i32 s38, 0, 0x1e400
	v_lshl_add_u64 v[0:1], v[14:15], 4, s[60:61]
	v_lshl_add_u32 v2, v14, 3, 0
	s_mov_b64 s[16:17], 0x31ce8000
	s_mov_b64 s[18:19], 0x31ef8000
	v_lshl_add_u32 v32, v14, 4, 0
	v_lshl_add_u64 v[16:17], v[0:1], 0, s[2:3]
	v_add_u32_e32 v37, 0x1c400, v2
	v_lshlrev_b64 v[2:3], 2, v[14:15]
	s_add_u32 s40, s60, 0x323f8000
	s_mov_b64 s[2:3], 0x353f8000
	v_cmp_gt_i32_e64 s[8:9], 16, v14
	v_lshl_add_u32 v30, v14, 2, s38
	v_and_b32_e32 v31, 15, v14
	v_add_u32_e32 v33, 0xfffff800, v14
	v_add_u32_e32 v34, 0x10000, v32
	v_lshl_add_u64 v[18:19], v[0:1], 0, s[16:17]
	v_add_u32_e32 v35, 0x18400, v32
	v_lshl_add_u64 v[20:21], v[0:1], 0, s[18:19]
	s_movk_i32 s39, 0xfe00
	v_add_u32_e32 v36, 0xfffffe00, v14
	s_waitcnt lgkmcnt(0)
	v_lshl_add_u64 v[22:23], s[12:13], 0, v[2:3]
	v_lshl_add_u64 v[24:25], s[14:15], 0, v[2:3]
	s_addc_u32 s41, s61, 0
	v_lshl_add_u64 v[26:27], v[0:1], 0, s[2:3]
	v_mov_b32_e32 v8, 0
	s_movk_i32 s42, 0x200
	s_movk_i32 s44, 0xe00
	s_movk_i32 s46, 0xc00
	s_movk_i32 s47, 0xa00
	s_mov_b64 s[2:3], 0x8000
	s_movk_i32 s48, 0x7ff
	s_movk_i32 s49, 0x640
	s_movk_i32 s50, 0x440
	s_movk_i32 s51, 0x240
	s_movk_i32 s52, 0xfbff
	s_mov_b64 s[16:17], 0x800
	s_movk_i32 s53, 0x1ff
	s_mov_b32 s54, 0x2aaaaaab
	s_movk_i32 s55, 0xffe0
	s_movk_i32 s56, 0x80
	s_mov_b32 s57, 0x1fffffc0
	s_movk_i32 s58, 0x108
	s_mov_b64 s[18:19], 0x2000
	s_movk_i32 s59, 0x2dff
	s_movk_i32 s62, 0xdff
	v_mov_b32_e32 v38, 0x8400
	s_mov_b32 s63, s94
	s_mov_b32 s64, s94
	s_branch .LBB0_221

.LBB0_340:
	v_readlane_b32 s0, v250, 4
	s_mov_b32 s0, s2
	v_writelane_b32 v255, s0, 33
	s_nop 1
	v_writelane_b32 v255, s1, 34
	s_mul_i32 s0, s2, 10
	s_add_i32 s4, s0, 3
	s_waitcnt lgkmcnt(0)
	s_mov_b32 s2, s100
	s_waitcnt lgkmcnt(0)
	s_mov_b32 s1, s101
	s_cmp_le_i32 s2, s4
	s_cselect_b64 s[2:3], -1, 0
	s_cmp_lt_i32 s4, s1
	s_cselect_b64 s[4:5], -1, 0
	s_and_b64 s[2:3], s[2:3], s[4:5]
	v_writelane_b32 v255, s0, 35
	s_and_b64 vcc, exec, s[2:3]
	s_mov_b64 s[2:3], -1
	s_cbranch_vccnz .LBB0_342
	v_readlane_b32 s0, v255, 35
	s_add_i32 s22, s0, 4
	s_mov_b64 s[2:3], 0

.LBB0_506:
	v_readlane_b32 s0, v250, 4
	s_waitcnt vmcnt(0)
	s_waitcnt lgkmcnt(0)
	s_mov_b32 s1, s100
	s_cmp_le_i32 s1, s22
	s_cselect_b64 s[2:3], -1, 0
	s_waitcnt lgkmcnt(0)
	s_mov_b32 s57, s101
	s_cmp_lt_i32 s22, s57
	s_cselect_b64 s[4:5], -1, 0
	s_and_b64 s[4:5], s[2:3], s[4:5]
	s_mov_b64 s[2:3], -1
	s_and_b64 vcc, exec, s[4:5]
	s_cbranch_vccnz .LBB0_508
	v_readlane_b32 s0, v255, 35
	s_add_i32 s1, s0, 5
	s_mov_b64 s[2:3], 0

.LBB0_638:
	v_readlane_b32 s0, v250, 4
	s_waitcnt lgkmcnt(0)
	s_mov_b32 s2, s100
	s_cmp_le_i32 s2, s1
	s_cselect_b64 s[2:3], -1, 0
	s_waitcnt lgkmcnt(0)
	s_mov_b32 s65, s101
	s_cmp_lt_i32 s1, s65
	s_cselect_b64 s[4:5], -1, 0
	s_and_b64 s[4:5], s[2:3], s[4:5]
	s_mov_b64 s[2:3], -1
	s_and_b64 vcc, exec, s[4:5]
	s_cbranch_vccnz .LBB0_640
	v_readlane_b32 s0, v255, 35
	s_add_i32 s1, s0, 6
	s_mov_b64 s[2:3], 0

.LBB0_875:
	v_readlane_b32 s0, v250, 4
	s_waitcnt lgkmcnt(0)
	s_mov_b32 s2, s100
	s_cmp_le_i32 s2, s1
	s_cselect_b64 s[2:3], -1, 0
	s_waitcnt lgkmcnt(0)
	s_mov_b32 s4, s101
	s_cmp_lt_i32 s1, s4
	s_cselect_b64 s[6:7], -1, 0
	s_and_b64 s[6:7], s[2:3], s[6:7]
	s_mov_b64 s[2:3], -1
	s_and_b64 vcc, exec, s[6:7]
	s_cbranch_vccnz .LBB0_877
	v_readlane_b32 s0, v255, 35
	s_add_i32 s1, s0, 7
	s_mov_b64 s[2:3], 0

.LBB0_1051:
	v_readlane_b32 s0, v250, 4
	s_waitcnt lgkmcnt(0)
	s_mov_b32 s2, s100
	s_cmp_le_i32 s2, s1
	s_cselect_b64 s[2:3], -1, 0
	s_waitcnt lgkmcnt(0)
	s_mov_b32 s28, s101
	s_cmp_lt_i32 s1, s28
	s_cselect_b64 s[4:5], -1, 0
	s_and_b64 s[4:5], s[2:3], s[4:5]
	s_mov_b64 s[2:3], -1
	s_and_b64 vcc, exec, s[4:5]
	s_cbranch_vccnz .LBB0_1053
	v_readlane_b32 s0, v255, 35
	s_add_i32 s1, s0, 8
	s_mov_b64 s[2:3], 0

.LBB0_1227:
	v_readlane_b32 s0, v250, 4
	s_waitcnt lgkmcnt(0)
	s_mov_b32 s2, s100
	s_cmp_le_i32 s2, s1
	s_cselect_b64 s[2:3], -1, 0
	s_waitcnt lgkmcnt(0)
	s_mov_b32 s4, s101
	s_cmp_lt_i32 s1, s4
	s_cselect_b64 s[6:7], -1, 0
	s_and_b64 s[6:7], s[2:3], s[6:7]
	s_mov_b64 s[2:3], -1
	s_and_b64 vcc, exec, s[6:7]
	s_cbranch_vccnz .LBB0_1229
	v_readlane_b32 s0, v255, 35
	s_add_i32 s1, s0, 9
	s_mov_b64 s[2:3], 0

.LBB0_1287:
	v_readlane_b32 s0, v250, 4
	s_waitcnt lgkmcnt(0)
	s_mov_b32 s2, s100
	s_cmp_le_i32 s2, s1
	s_cselect_b64 s[2:3], -1, 0
	s_waitcnt lgkmcnt(0)
	s_mov_b32 s25, s101
	s_cmp_lt_i32 s1, s25
	s_cselect_b64 s[4:5], -1, 0
	s_and_b64 s[4:5], s[2:3], s[4:5]
	s_mov_b64 s[2:3], -1
	s_and_b64 vcc, exec, s[4:5]
	s_cbranch_vccnz .LBB0_1289
	v_readlane_b32 s0, v255, 35
	s_add_i32 s1, s0, 10
	s_mov_b64 s[2:3], 0

.LBB0_1384:
	v_readlane_b32 s0, v250, 4
	s_waitcnt lgkmcnt(0)
	s_mov_b32 s2, s100
	s_cmp_le_i32 s2, s1
	s_cselect_b64 s[2:3], -1, 0
	s_waitcnt lgkmcnt(0)
	s_mov_b32 s12, s101
	s_cmp_lt_i32 s1, s12
	s_cselect_b64 s[4:5], -1, 0
	s_and_b64 s[4:5], s[2:3], s[4:5]
	s_mov_b64 s[2:3], -1
	s_and_b64 vcc, exec, s[4:5]
	s_cbranch_vccnz .LBB0_1386
	v_readlane_b32 s0, v255, 35
	s_add_i32 s1, s0, 11
	s_mov_b64 s[2:3], 0

.LBB0_1503:
	v_readlane_b32 s0, v250, 4
	s_waitcnt lgkmcnt(0)
	s_mov_b32 s2, s100
	s_cmp_le_i32 s2, s1
	s_cselect_b64 s[2:3], -1, 0
	s_waitcnt lgkmcnt(0)
	s_mov_b32 s28, s101
	s_cmp_lt_i32 s1, s28
	s_cselect_b64 s[4:5], -1, 0
	s_and_b64 s[4:5], s[2:3], s[4:5]
	s_mov_b64 s[2:3], -1
	s_and_b64 vcc, exec, s[4:5]
	s_cbranch_vccnz .LBB0_1505
	v_readlane_b32 s0, v255, 35
	s_add_i32 s22, s0, 12
	s_mov_b64 s[2:3], 0

.LBB0_1620:
	v_readlane_b32 s0, v250, 4
	s_waitcnt lgkmcnt(0)
	s_mov_b32 s2, s100
	s_cmp_le_i32 s2, s22
	s_cselect_b64 s[2:3], -1, 0
	s_waitcnt lgkmcnt(0)
	s_mov_b32 s1, s101
	s_cmp_lt_i32 s22, s1
	s_cselect_b64 s[4:5], -1, 0
	s_and_b64 s[2:3], s[2:3], s[4:5]
	s_andn2_b64 vcc, exec, s[2:3]
	s_cbranch_vccz .LBB0_1621
	s_getpc_b64 s[98:99]

.LBB0_1727:
	v_readlane_b32 s0, v250, 4
	s_waitcnt lgkmcnt(0)
	s_mov_b32 s0, s100
	s_cmp_lt_i32 s0, 44
	s_mov_b32 s21, s101
	s_cselect_b64 s[0:1], -1, 0
	s_cmp_gt_i32 s21, 43
	s_cselect_b64 s[2:3], -1, 0
	s_and_b64 s[0:1], s[0:1], s[2:3]
	s_and_b64 vcc, exec, s[0:1]
	s_cbranch_vccz .LBB0_1826
	v_mbcnt_lo_u32_b32 v2, -1, 0
	v_mbcnt_hi_u32_b32 v2, -1, v2
	v_lshl_add_u32 v3, s43, 6, v2
	s_nop 0
	v_readlane_b32 s10, v255, 17
	v_readlane_b32 s38, v252, 10
	v_readlane_b32 s11, v255, 18
	v_readlane_b32 s39, v252, 11
	v_lshlrev_b32_e32 v0, 2, v3
	v_add_u32_e32 v1, 0x20000, v0
	ds_read_b32 v1, v1
	s_waitcnt lgkmcnt(0)
	ds_write_b32 v0, v1
	s_add_i32 s0, s37, 0x3fff
	s_ashr_i32 s1, s0, 31
	v_readlane_b32 s2, v252, 0
	s_xor_b32 s1, s1, s2
	s_sub_i32 s2, 0xffffc001, s37
	s_max_i32 s0, s0, s2
	v_readlane_b32 s2, v252, 33
	s_mul_hi_u32 s2, s0, s2
	v_readlane_b32 s5, v252, 34
	s_mul_i32 s3, s2, s5
	s_sub_i32 s0, s0, s3
	s_add_i32 s3, s2, 1
	s_sub_i32 s4, s0, s5
	s_cmp_ge_u32 s0, s5
	s_cselect_b32 s2, s3, s2
	s_cselect_b32 s0, s4, s0
	s_add_i32 s3, s2, 1
	s_cmp_ge_u32 s0, s5
	s_cselect_b32 s0, s3, s2
	s_xor_b32 s0, s0, s1
	s_sub_i32 s0, s0, s1
	s_mul_i32 s8, s0, s94
	s_add_i32 s1, s8, 0x800
	s_add_i32 s0, s1, s0
	s_min_i32 s2, s0, 0x4800
	s_add_i32 s0, s1, s43
	s_cmp_ge_i32 s0, s2
	s_waitcnt lgkmcnt(0)
	s_barrier
	s_cbranch_scc1 .LBB0_1772
	s_min_i32 s1, s1, 0x47ff
	s_load_dwordx4 s[4:7], s[10:11], 0x118
	s_addk_i32 s1, 0xf800
	s_add_i32 s3, s2, -1
	s_lshr_b32 s1, s1, 11
	v_lshlrev_b32_e32 v80, 2, v2
	s_cmp_gt_i32 s8, -1
	v_ashrrev_i32_e32 v81, 31, v80
	s_cselect_b32 s33, s1, 8
	v_lshlrev_b64 v[48:49], 2, v[80:81]
	s_add_i32 s1, s33, 27
	s_waitcnt lgkmcnt(0)
	v_lshl_add_u64 v[16:17], s[4:5], 0, v[48:49]
	s_mul_hi_u32 s5, s1, 0x6000
	s_mulk_i32 s1, 0x6000
	s_add_u32 s4, s84, s1
	s_addc_u32 s5, s86, s5
	s_add_i32 s1, s0, 8
	global_load_dwordx4 v[0:3], v[16:17], off
	global_load_dwordx4 v[4:7], v[16:17], off offset:1024
	global_load_dwordx4 v[8:11], v[16:17], off offset:2048
	global_load_dwordx4 v[12:15], v[16:17], off offset:3072
	v_lshl_add_u64 v[16:17], s[4:5], 0, v[48:49]
	s_min_i32 s4, s1, s3
	s_ashr_i32 s5, s4, 31
	s_lshl_b64 s[4:5], s[4:5], 4
	s_add_u32 s10, s38, s4
	s_addc_u32 s11, s39, s5
	s_add_u32 s4, s90, s4
	v_mov_b32_e32 v106, 0
	s_addc_u32 s5, s91, s5
	s_ashr_i32 s1, s0, 31
	global_load_dwordx4 v[40:43], v106, s[10:11]
	global_load_dwordx4 v[32:35], v106, s[4:5]
	s_lshl_b64 s[4:5], s[0:1], 4
	s_add_u32 s10, s38, s4
	s_mov_b64 s[16:17], 0x5000
	s_movk_i32 s9, 0x5000
	s_addc_u32 s11, s39, s5
	v_lshl_add_u64 v[50:51], v[16:17], 0, s[16:17]
	s_add_u32 s4, s90, s4
	v_add_co_u32_e32 v52, vcc, s9, v16
	s_addc_u32 s5, s91, s5
	global_load_dwordx4 v[44:47], v106, s[10:11]
	global_load_dwordx4 v[36:39], v106, s[4:5]
	v_addc_co_u32_e32 v53, vcc, 0, v17, vcc
	global_load_dwordx4 v[16:19], v[50:51], off offset:1024
	global_load_dwordx4 v[20:23], v[50:51], off offset:2048
	global_load_dwordx4 v[24:27], v[52:53], off
	global_load_dwordx4 v[28:31], v[50:51], off offset:3072
	s_add_i32 s24, s43, s8
	s_lshl_b64 s[0:1], s[0:1], 11
	s_add_u32 s0, s60, s0
	v_lshlrev_b64 v[50:51], 1, v[80:81]
	v_readlane_b32 s10, v250, 5
	s_addc_u32 s1, s61, s1
	s_mov_b64 s[4:5], 0x3ad38000
	v_readlane_b32 s11, v250, 6
	v_lshl_add_u64 v[84:85], s[6:7], 0, v[48:49]
	v_lshl_add_u64 v[48:49], s[0:1], 0, v[50:51]
	s_mov_b32 s19, 0
	s_mov_b32 s20, 0x3e000000
	v_mov_b32_e32 v107, 0x358637bd
	s_mov_b32 s34, 0x800000
	s_mov_b64 s[22:23], 0x8000
	v_lshl_add_u64 v[82:83], s[10:11], 0, v[50:51]
	v_lshl_add_u64 v[86:87], v[48:49], 0, s[4:5]
	v_mov_b32_e32 v108, 0x3a800000
	s_waitcnt vmcnt(6)
	v_readfirstlane_b32 s12, v32
	v_readfirstlane_b32 s13, v33
	v_readfirstlane_b32 s14, v34
	v_readfirstlane_b32 s15, v35
	s_waitcnt vmcnt(4)
	v_readfirstlane_b32 s4, v36
	v_readfirstlane_b32 s5, v37
	v_readfirstlane_b32 s6, v38
	v_readfirstlane_b32 s7, v39
	s_branch .LBB0_1754

	.amdhsa_kernel _Z6mk_fwd6Params
		.amdhsa_group_segment_fixed_size 0
		.amdhsa_private_segment_fixed_size 0
		.amdhsa_kernarg_size 568
		.amdhsa_user_sgpr_count 2
		.amdhsa_user_sgpr_dispatch_ptr 0
		.amdhsa_user_sgpr_queue_ptr 0
		.amdhsa_user_sgpr_kernarg_segment_ptr 1
		.amdhsa_user_sgpr_dispatch_id 0
		.amdhsa_user_sgpr_kernarg_preload_length 0
		.amdhsa_user_sgpr_kernarg_preload_offset 0
		.amdhsa_user_sgpr_private_segment_size 0
		.amdhsa_uses_dynamic_stack 0
		.amdhsa_enable_private_segment 0
		.amdhsa_system_sgpr_workgroup_id_x 1
		.amdhsa_system_sgpr_workgroup_id_y 0
		.amdhsa_system_sgpr_workgroup_id_z 0
		.amdhsa_system_sgpr_workgroup_info 0
		.amdhsa_system_vgpr_workitem_id 0
		.amdhsa_next_free_vgpr 256
		.amdhsa_next_free_sgpr 102
		.amdhsa_accum_offset 256
		.amdhsa_reserve_vcc 1
		.amdhsa_float_round_mode_32 0
		.amdhsa_float_round_mode_16_64 0
		.amdhsa_float_denorm_mode_32 3
		.amdhsa_float_denorm_mode_16_64 3
		.amdhsa_dx10_clamp 1
		.amdhsa_ieee_mode 1
		.amdhsa_fp16_overflow 0
		.amdhsa_tg_split 0
		.amdhsa_exception_fp_ieee_invalid_op 0
		.amdhsa_exception_fp_denorm_src 0
		.amdhsa_exception_fp_ieee_div_zero 0
		.amdhsa_exception_fp_ieee_overflow 0
		.amdhsa_exception_fp_ieee_underflow 0
		.amdhsa_exception_fp_ieee_inexact 0
		.amdhsa_exception_int_div_zero 0
	.end_amdhsa_kernel

amdhsa.kernels:
  - .agpr_count:     0
    .args:
      - .offset:         0
        .size:           312
        .value_kind:     by_value
      - .offset:         312
        .size:           4
        .value_kind:     hidden_block_count_x
      - .offset:         316
        .size:           4
        .value_kind:     hidden_block_count_y
      - .offset:         320
        .size:           4
        .value_kind:     hidden_block_count_z
      - .offset:         324
        .size:           2
        .value_kind:     hidden_group_size_x
      - .offset:         326
        .size:           2
        .value_kind:     hidden_group_size_y
      - .offset:         328
        .size:           2
        .value_kind:     hidden_group_size_z
      - .offset:         330
        .size:           2
        .value_kind:     hidden_remainder_x
      - .offset:         332
        .size:           2
        .value_kind:     hidden_remainder_y
      - .offset:         334
        .size:           2
        .value_kind:     hidden_remainder_z
      - .offset:         352
        .size:           8
        .value_kind:     hidden_global_offset_x
      - .offset:         360
        .size:           8
        .value_kind:     hidden_global_offset_y
      - .offset:         368
        .size:           8
        .value_kind:     hidden_global_offset_z
      - .offset:         376
        .size:           2
        .value_kind:     hidden_grid_dims
      - .offset:         432
        .size:           4
        .value_kind:     hidden_dynamic_lds_size
    .group_segment_fixed_size: 0
    .kernarg_segment_align: 8
    .kernarg_segment_size: 568
    .language:       OpenCL C
    .language_version:
      - 2
      - 0
    .max_flat_workgroup_size: 512
    .name:           _Z6mk_fwd6Params
    .private_segment_fixed_size: 0
    .sgpr_count:     108
    .sgpr_spill_count: 379
    .symbol:         _Z6mk_fwd6Params.kd
    .uniform_work_group_size: 1
    .uses_dynamic_stack: false
    .vgpr_count:     256
    .vgpr_spill_count: 0
    .wavefront_size: 64
